# static priority: layer-2 gather phase at s_setprio 2, epilogue back to 0
# speedup vs baseline: 1.0209x; 1.0065x over previous
.LBB2_350:
	v_readfirstlane_b32 s91, v0
	v_and_b32_e32 v1, 0x3c0, v0
	s_lshr_b32 s91, s91, 6
	s_movk_i32 s0, 0x31f
	v_cmp_gt_u32_e32 vcc, s0, v1
	s_and_saveexec_b64 s[0:1], vcc
	s_cbranch_execz .LBB2_371
	s_setprio 2
	s_andn2_b64 vcc, exec, s[4:5]
	s_cbranch_vccnz .LBB2_365
	v_add_u32_e32 v1, 8, v46
	v_mov_b32_e32 v43, 0x3f80
	v_mov_b32_e32 v42, 1.0
	v_cmp_le_u32_e32 vcc, v1, v47
	v_mov_b32_e32 v7, 0
	v_mov_b32_e32 v6, 0
	v_mov_b32_e32 v9, 0
	v_mov_b32_e32 v8, 0
	v_mov_b32_e32 v3, 0
	v_mov_b32_e32 v2, 0
	v_mov_b32_e32 v5, 0
	v_mov_b32_e32 v4, 0
	s_and_saveexec_b64 s[0:1], vcc
	s_cbranch_execz .LBB2_356
	v_mov_b32_e32 v1, v44
	v_lshlrev_b32_e32 v45, 2, v46
	v_mov_b32_e32 v5, 0
	s_mov_b64 s[2:3], 0
	v_mov_b32_e32 v4, 0
	v_mov_b32_e32 v3, 0
	v_mov_b32_e32 v2, 0
	v_mov_b32_e32 v9, 0
	v_mov_b32_e32 v8, 0
	v_mov_b32_e32 v7, 0
	v_mov_b32_e32 v6, 0

.LBB2_369:
	s_setprio 0
	v_xor_b32_e32 v0, 1, v51
	v_add_u32_e32 v1, 64, v52
	v_cmp_lt_i32_e32 vcc, v0, v1
	s_waitcnt lgkmcnt(0)
	v_mul_f32_e32 v2, v53, v2
	v_cndmask_b32_e32 v0, v51, v0, vcc
	v_lshlrev_b32_e32 v65, 2, v0
	v_mul_f32_e32 v0, v53, v6
	s_nop 1
	v_mov_b32_dpp v1, v0 quad_perm:[1,0,3,2] row_mask:0xf bank_mask:0xf
	v_cmp_eq_u32_e32 vcc, 0, v44
	v_mul_f32_e32 v6, v53, v7
	s_nop 1
	v_mov_b32_dpp v7, v6 quad_perm:[1,0,3,2] row_mask:0xf bank_mask:0xf
	s_waitcnt lgkmcnt(1)
	v_cndmask_b32_e32 v52, v1, v0, vcc
	v_cndmask_b32_e32 v70, v0, v1, vcc
	v_mul_f32_e32 v0, v53, v8
	s_nop 1
	v_mov_b32_dpp v1, v0 quad_perm:[1,0,3,2] row_mask:0xf bank_mask:0xf
	s_nop 1
	v_mov_b32_dpp v8, v2 quad_perm:[1,0,3,2] row_mask:0xf bank_mask:0xf
	s_waitcnt lgkmcnt(2)
	v_cndmask_b32_e32 v54, v7, v6, vcc
	v_cndmask_b32_e32 v68, v6, v7, vcc
	v_mul_f32_e32 v6, v53, v9
	s_waitcnt lgkmcnt(1)
	v_cndmask_b32_e32 v56, v1, v0, vcc
	v_cndmask_b32_e32 v76, v0, v1, vcc
	v_mul_f32_e32 v0, v53, v3
	s_nop 1
	v_mov_b32_dpp v1, v0 quad_perm:[1,0,3,2] row_mask:0xf bank_mask:0xf
	s_waitcnt lgkmcnt(1)
	v_cndmask_b32_e32 v60, v8, v2, vcc
	v_cndmask_b32_e32 v72, v2, v8, vcc
	v_mul_f32_e32 v2, v53, v4
	v_mul_f32_e32 v4, v53, v5
	s_nop 1
	v_mov_b32_dpp v5, v4 quad_perm:[1,0,3,2] row_mask:0xf bank_mask:0xf
	s_nop 1
	v_mov_b32_dpp v3, v2 quad_perm:[1,0,3,2] row_mask:0xf bank_mask:0xf
	s_nop 1
	v_mov_b32_dpp v7, v6 quad_perm:[1,0,3,2] row_mask:0xf bank_mask:0xf
	s_waitcnt lgkmcnt(3)
	v_cndmask_b32_e32 v62, v1, v0, vcc
	v_cndmask_b32_e32 v82, v0, v1, vcc
	v_mul_u32_u24_e32 v0, 20, v44
	v_lshlrev_b32_e32 v66, 2, v0
	s_waitcnt lgkmcnt(2)
	v_cndmask_b32_e32 v84, v5, v4, vcc
	v_cndmask_b32_e32 v78, v4, v5, vcc
	v_add_u32_e32 v66, 0x16400, v66
	s_waitcnt lgkmcnt(1)
	v_cndmask_b32_e32 v86, v3, v2, vcc
	v_cndmask_b32_e32 v80, v2, v3, vcc
	ds_read_b128 v[48:51], v66 offset:6224
	ds_read_b128 v[88:91], v66 offset:6240
	ds_read_b128 v[32:35], v66 offset:6256
	ds_read_b128 v[16:19], v66 offset:6272
	ds_read_b128 v[0:3], v66 offset:6288
	ds_read_b128 v[92:95], v66
	ds_read_b128 v[96:99], v66 offset:16
	ds_read_b128 v[40:43], v66 offset:32
	s_waitcnt lgkmcnt(8)
	v_cndmask_b32_e32 v58, v7, v6, vcc
	v_cndmask_b32_e32 v74, v6, v7, vcc
	ds_read_b128 v[20:23], v66 offset:48
	ds_read_b128 v[4:7], v66 offset:64
	ds_read_b128 v[100:103], v66 offset:160
	ds_read_b128 v[104:107], v66 offset:176
	ds_read_b128 v[36:39], v66 offset:192
	ds_read_b128 v[24:27], v66 offset:208
	s_waitcnt vmcnt(0)
	ds_read_b128 v[8:11], v66 offset:224
	ds_read_b128 v[108:111], v66 offset:320
	ds_read_b128 v[112:115], v66 offset:336
	ds_read_b128 v[44:47], v66 offset:352
	ds_read_b128 v[28:31], v66 offset:368
	ds_read_b128 v[12:15], v66 offset:384
	s_waitcnt lgkmcnt(14)
	v_pk_fma_f32 v[48:49], v[52:53], v[92:93], v[48:49] op_sel_hi:[0,1,1]
	v_pk_fma_f32 v[50:51], v[52:53], v[94:95], v[50:51] op_sel_hi:[0,1,1]
	ds_read_b128 v[92:95], v66 offset:480
	ds_read_b128 v[116:119], v66 offset:496
	s_waitcnt lgkmcnt(11)
	v_pk_fma_f32 v[48:49], v[54:55], v[100:101], v[48:49] op_sel_hi:[0,1,1]
	v_pk_fma_f32 v[50:51], v[54:55], v[102:103], v[50:51] op_sel_hi:[0,1,1]
	ds_read_b128 v[120:123], v66 offset:512
	ds_read_b128 v[124:127], v66 offset:528
	s_waitcnt lgkmcnt(8)
	v_pk_fma_f32 v[100:101], v[56:57], v[108:109], v[48:49] op_sel_hi:[0,1,1]
	v_pk_fma_f32 v[102:103], v[56:57], v[110:111], v[50:51] op_sel_hi:[0,1,1]
	v_pk_fma_f32 v[96:97], v[52:53], v[96:97], v[88:89] op_sel_hi:[0,1,1]
	v_pk_fma_f32 v[108:109], v[52:53], v[98:99], v[90:91] op_sel_hi:[0,1,1]
	ds_read_b128 v[48:51], v66 offset:544
	ds_read_b128 v[88:91], v66 offset:640
	s_waitcnt lgkmcnt(5)
	v_pk_fma_f32 v[98:99], v[58:59], v[92:93], v[100:101] op_sel_hi:[0,1,1]
	v_pk_fma_f32 v[100:101], v[58:59], v[94:95], v[102:103] op_sel_hi:[0,1,1]
	ds_read_b128 v[92:95], v66 offset:800
	s_waitcnt lgkmcnt(1)
	v_pk_fma_f32 v[98:99], v[60:61], v[88:89], v[98:99] op_sel_hi:[0,1,1]
	v_pk_fma_f32 v[100:101], v[60:61], v[90:91], v[100:101] op_sel_hi:[0,1,1]
	ds_read_b128 v[88:91], v66 offset:816
	s_waitcnt lgkmcnt(1)
	v_pk_fma_f32 v[98:99], v[62:63], v[92:93], v[98:99] op_sel_hi:[0,1,1]
	v_pk_fma_f32 v[92:93], v[62:63], v[94:95], v[100:101] op_sel_hi:[0,1,1]
	v_pk_fma_f32 v[100:101], v[54:55], v[104:105], v[96:97] op_sel_hi:[0,1,1]
	v_pk_fma_f32 v[102:103], v[54:55], v[106:107], v[108:109] op_sel_hi:[0,1,1]
	ds_read_b128 v[94:97], v66 offset:656
	ds_read_b128 v[108:111], v66 offset:672
	v_pk_fma_f32 v[100:101], v[56:57], v[112:113], v[100:101] op_sel_hi:[0,1,1]
	v_pk_fma_f32 v[102:103], v[56:57], v[114:115], v[102:103] op_sel_hi:[0,1,1]
	v_pk_fma_f32 v[100:101], v[58:59], v[116:117], v[100:101] op_sel_hi:[0,1,1]
	v_pk_fma_f32 v[102:103], v[58:59], v[118:119], v[102:103] op_sel_hi:[0,1,1]
	ds_read_b128 v[112:115], v66 offset:688
	ds_read_b128 v[116:119], v66 offset:704
	v_pk_fma_f32 v[32:33], v[52:53], v[40:41], v[32:33] op_sel_hi:[0,1,1]
	v_pk_fma_f32 v[32:33], v[54:55], v[36:37], v[32:33] op_sel_hi:[0,1,1]
	v_pk_fma_f32 v[32:33], v[56:57], v[44:45], v[32:33] op_sel_hi:[0,1,1]
	s_waitcnt lgkmcnt(3)
	v_pk_fma_f32 v[94:95], v[60:61], v[94:95], v[100:101] op_sel_hi:[0,1,1]
	v_pk_fma_f32 v[32:33], v[58:59], v[120:121], v[32:33] op_sel_hi:[0,1,1]
	v_pk_fma_f32 v[106:107], v[62:63], v[88:89], v[94:95] op_sel_hi:[0,1,1]
	v_pk_fma_f32 v[88:89], v[60:61], v[96:97], v[102:103] op_sel_hi:[0,1,1]
	s_waitcnt lgkmcnt(2)
	v_pk_fma_f32 v[36:37], v[60:61], v[108:109], v[32:33] op_sel_hi:[0,1,1]
	v_pk_fma_f32 v[104:105], v[62:63], v[90:91], v[88:89] op_sel_hi:[0,1,1]
	ds_read_b128 v[88:91], v66 offset:832
	v_pk_fma_f32 v[40:41], v[52:53], v[42:43], v[34:35] op_sel_hi:[0,1,1]
	ds_read_b128 v[32:35], v66 offset:848
	v_pk_fma_f32 v[16:17], v[52:53], v[20:21], v[16:17] op_sel_hi:[0,1,1]
	v_pk_fma_f32 v[16:17], v[54:55], v[24:25], v[16:17] op_sel_hi:[0,1,1]
	v_pk_fma_f32 v[16:17], v[56:57], v[28:29], v[16:17] op_sel_hi:[0,1,1]
	v_pk_fma_f32 v[16:17], v[58:59], v[124:125], v[16:17] op_sel_hi:[0,1,1]
	s_waitcnt lgkmcnt(3)
	v_pk_fma_f32 v[16:17], v[60:61], v[112:113], v[16:17] op_sel_hi:[0,1,1]
	s_waitcnt lgkmcnt(1)
	v_pk_fma_f32 v[102:103], v[62:63], v[88:89], v[36:37] op_sel_hi:[0,1,1]
	s_waitcnt lgkmcnt(0)
	v_pk_fma_f32 v[88:89], v[62:63], v[32:33], v[16:17] op_sel_hi:[0,1,1]
	v_pk_fma_f32 v[16:17], v[52:53], v[22:23], v[18:19] op_sel_hi:[0,1,1]
	v_pk_fma_f32 v[16:17], v[54:55], v[26:27], v[16:17] op_sel_hi:[0,1,1]
	v_pk_fma_f32 v[16:17], v[56:57], v[30:31], v[16:17] op_sel_hi:[0,1,1]
	v_pk_fma_f32 v[16:17], v[58:59], v[126:127], v[16:17] op_sel_hi:[0,1,1]
	v_pk_fma_f32 v[16:17], v[60:61], v[114:115], v[16:17] op_sel_hi:[0,1,1]
	v_pk_fma_f32 v[94:95], v[62:63], v[34:35], v[16:17] op_sel_hi:[0,1,1]
	ds_read_b128 v[16:19], v66 offset:864
	v_pk_fma_f32 v[0:1], v[52:53], v[4:5], v[0:1] op_sel_hi:[0,1,1]
	v_pk_fma_f32 v[0:1], v[54:55], v[8:9], v[0:1] op_sel_hi:[0,1,1]
	v_pk_fma_f32 v[0:1], v[56:57], v[12:13], v[0:1] op_sel_hi:[0,1,1]
	v_pk_fma_f32 v[0:1], v[58:59], v[48:49], v[0:1] op_sel_hi:[0,1,1]
	v_pk_fma_f32 v[0:1], v[60:61], v[116:117], v[0:1] op_sel_hi:[0,1,1]
	ds_read_b128 v[32:35], v66 offset:960
	s_waitcnt lgkmcnt(1)
	v_pk_fma_f32 v[96:97], v[62:63], v[16:17], v[0:1] op_sel_hi:[0,1,1]
	v_pk_fma_f32 v[0:1], v[52:53], v[6:7], v[2:3] op_sel_hi:[0,1,1]
	v_pk_fma_f32 v[36:37], v[54:55], v[38:39], v[40:41] op_sel_hi:[0,1,1]
	v_pk_fma_f32 v[0:1], v[54:55], v[10:11], v[0:1] op_sel_hi:[0,1,1]
	v_pk_fma_f32 v[36:37], v[56:57], v[46:47], v[36:37] op_sel_hi:[0,1,1]
	v_pk_fma_f32 v[0:1], v[56:57], v[14:15], v[0:1] op_sel_hi:[0,1,1]
	v_pk_fma_f32 v[36:37], v[58:59], v[122:123], v[36:37] op_sel_hi:[0,1,1]
	v_pk_fma_f32 v[0:1], v[58:59], v[50:51], v[0:1] op_sel_hi:[0,1,1]
	v_pk_fma_f32 v[36:37], v[60:61], v[110:111], v[36:37] op_sel_hi:[0,1,1]
	v_pk_fma_f32 v[0:1], v[60:61], v[118:119], v[0:1] op_sel_hi:[0,1,1]
	v_pk_fma_f32 v[100:101], v[62:63], v[90:91], v[36:37] op_sel_hi:[0,1,1]
	v_pk_fma_f32 v[90:91], v[62:63], v[18:19], v[0:1] op_sel_hi:[0,1,1]
	ds_read_b128 v[48:51], v66 offset:976
	ds_read_b128 v[28:31], v66 offset:992
	ds_read_b128 v[16:19], v66 offset:1008
	ds_read_b128 v[0:3], v66 offset:1024
	ds_read_b128 v[44:47], v66 offset:1120
	ds_read_b128 v[52:55], v66 offset:1136
	ds_read_b128 v[36:39], v66 offset:1152
	ds_read_b128 v[20:23], v66 offset:1168
	ds_read_b128 v[4:7], v66 offset:1184
	ds_read_b128 v[108:111], v66 offset:1280
	ds_read_b128 v[56:59], v66 offset:1296
	ds_read_b128 v[40:43], v66 offset:1312
	ds_read_b128 v[24:27], v66 offset:1328
	ds_read_b128 v[8:11], v66 offset:1344
	ds_read_b128 v[112:115], v66 offset:1440
	ds_read_b128 v[60:63], v66 offset:1456
	ds_read_b128 v[12:15], v66 offset:1504
	ds_read_b128 v[116:119], v66 offset:1600
	s_waitcnt lgkmcnt(14)
	v_pk_fma_f32 v[32:33], v[86:87], v[32:33], v[98:99] op_sel_hi:[0,1,1]
	v_pk_fma_f32 v[34:35], v[86:87], v[34:35], v[92:93] op_sel_hi:[0,1,1]
	s_waitcnt lgkmcnt(13)
	v_pk_fma_f32 v[32:33], v[84:85], v[44:45], v[32:33] op_sel_hi:[0,1,1]
	v_pk_fma_f32 v[34:35], v[84:85], v[46:47], v[34:35] op_sel_hi:[0,1,1]
	ds_read_b128 v[120:123], v66 offset:1760
	ds_read_b128 v[124:127], v66 offset:1776
	s_waitcnt lgkmcnt(10)
	v_pk_fma_f32 v[92:93], v[70:71], v[108:109], v[32:33] op_sel_hi:[0,1,1]
	v_pk_fma_f32 v[98:99], v[70:71], v[110:111], v[34:35] op_sel_hi:[0,1,1]
	ds_read_b128 v[32:35], v66 offset:1824
	ds_read_b128 v[44:47], v66 offset:1920
	s_waitcnt lgkmcnt(7)
	v_pk_fma_f32 v[92:93], v[68:69], v[112:113], v[92:93] op_sel_hi:[0,1,1]
	v_pk_fma_f32 v[98:99], v[68:69], v[114:115], v[98:99] op_sel_hi:[0,1,1]
	ds_read_b128 v[108:111], v66 offset:2080
	ds_read_b128 v[112:115], v66 offset:2096
	s_waitcnt lgkmcnt(6)
	v_pk_fma_f32 v[92:93], v[76:77], v[116:117], v[92:93] op_sel_hi:[0,1,1]
	v_pk_fma_f32 v[98:99], v[76:77], v[118:119], v[98:99] op_sel_hi:[0,1,1]
	s_waitcnt lgkmcnt(5)
	v_pk_fma_f32 v[92:93], v[74:75], v[120:121], v[92:93] op_sel_hi:[0,1,1]
	v_pk_fma_f32 v[98:99], v[74:75], v[122:123], v[98:99] op_sel_hi:[0,1,1]
	s_waitcnt lgkmcnt(2)
	v_pk_fma_f32 v[92:93], v[72:73], v[44:45], v[92:93] op_sel_hi:[0,1,1]
	v_pk_fma_f32 v[98:99], v[72:73], v[46:47], v[98:99] op_sel_hi:[0,1,1]
	ds_read_b128 v[44:47], v66 offset:2144
	ds_read_b128 v[116:119], v66 offset:2240
	s_waitcnt lgkmcnt(3)
	v_pk_fma_f32 v[92:93], v[82:83], v[108:109], v[92:93] op_sel_hi:[0,1,1]
	v_pk_fma_f32 v[98:99], v[82:83], v[110:111], v[98:99] op_sel_hi:[0,1,1]
	ds_read_b128 v[108:111], v66 offset:2400
	s_waitcnt lgkmcnt(1)
	v_pk_fma_f32 v[92:93], v[80:81], v[116:117], v[92:93] op_sel_hi:[0,1,1]
	v_pk_fma_f32 v[98:99], v[80:81], v[118:119], v[98:99] op_sel_hi:[0,1,1]
	s_waitcnt lgkmcnt(0)
	v_pk_fma_f32 v[92:93], v[78:79], v[108:109], v[92:93] op_sel_hi:[0,1,1]
	v_pk_fma_f32 v[98:99], v[78:79], v[110:111], v[98:99] op_sel_hi:[0,1,1]
	v_pk_fma_f32 v[108:109], v[86:87], v[48:49], v[106:107] op_sel_hi:[0,1,1]
	v_pk_fma_f32 v[110:111], v[86:87], v[50:51], v[104:105] op_sel_hi:[0,1,1]
	ds_read_b128 v[116:119], v66 offset:2416
	ds_read_b128 v[104:107], v66 offset:1472
	ds_read_b128 v[48:51], v66 offset:1488
	v_pk_fma_f32 v[52:53], v[84:85], v[52:53], v[108:109] op_sel_hi:[0,1,1]
	v_pk_fma_f32 v[54:55], v[84:85], v[54:55], v[110:111] op_sel_hi:[0,1,1]
	v_pk_fma_f32 v[56:57], v[70:71], v[56:57], v[52:53] op_sel_hi:[0,1,1]
	v_pk_fma_f32 v[58:59], v[70:71], v[58:59], v[54:55] op_sel_hi:[0,1,1]
	ds_read_b128 v[52:55], v66 offset:1616
	ds_read_b128 v[108:111], v66 offset:1632
	v_pk_fma_f32 v[56:57], v[68:69], v[60:61], v[56:57] op_sel_hi:[0,1,1]
	v_pk_fma_f32 v[58:59], v[68:69], v[62:63], v[58:59] op_sel_hi:[0,1,1]
	s_waitcnt lgkmcnt(1)
	v_pk_fma_f32 v[56:57], v[76:77], v[52:53], v[56:57] op_sel_hi:[0,1,1]
	v_pk_fma_f32 v[58:59], v[76:77], v[54:55], v[58:59] op_sel_hi:[0,1,1]
	ds_read_b128 v[52:55], v66 offset:1936
	v_pk_fma_f32 v[56:57], v[74:75], v[124:125], v[56:57] op_sel_hi:[0,1,1]
	v_pk_fma_f32 v[58:59], v[74:75], v[126:127], v[58:59] op_sel_hi:[0,1,1]
	ds_read_b128 v[60:63], v66 offset:1952
	s_waitcnt lgkmcnt(1)
	v_pk_fma_f32 v[56:57], v[72:73], v[52:53], v[56:57] op_sel_hi:[0,1,1]
	v_pk_fma_f32 v[58:59], v[72:73], v[54:55], v[58:59] op_sel_hi:[0,1,1]
	ds_read_b128 v[52:55], v66 offset:2256
	v_pk_fma_f32 v[56:57], v[82:83], v[112:113], v[56:57] op_sel_hi:[0,1,1]
	v_pk_fma_f32 v[58:59], v[82:83], v[114:115], v[58:59] op_sel_hi:[0,1,1]
	s_waitcnt lgkmcnt(0)
	v_pk_fma_f32 v[56:57], v[80:81], v[52:53], v[56:57] op_sel_hi:[0,1,1]
	v_pk_fma_f32 v[58:59], v[80:81], v[54:55], v[58:59] op_sel_hi:[0,1,1]
	v_pk_fma_f32 v[56:57], v[78:79], v[116:117], v[56:57] op_sel_hi:[0,1,1]
	v_pk_fma_f32 v[58:59], v[78:79], v[118:119], v[58:59] op_sel_hi:[0,1,1]
	v_pk_fma_f32 v[116:117], v[86:87], v[28:29], v[102:103] op_sel_hi:[0,1,1]
	v_pk_fma_f32 v[118:119], v[86:87], v[30:31], v[100:101] op_sel_hi:[0,1,1]
	ds_read_b128 v[112:115], v66 offset:2272
	ds_read_b128 v[120:123], v66 offset:1648
	ds_read_b128 v[52:55], v66 offset:1664
	v_pk_fma_f32 v[36:37], v[84:85], v[36:37], v[116:117] op_sel_hi:[0,1,1]
	v_pk_fma_f32 v[38:39], v[84:85], v[38:39], v[118:119] op_sel_hi:[0,1,1]
	ds_read_b128 v[28:31], v66 offset:1792
	ds_read_b128 v[100:103], v66 offset:1808
	v_pk_fma_f32 v[116:117], v[70:71], v[40:41], v[36:37] op_sel_hi:[0,1,1]
	v_pk_fma_f32 v[118:119], v[70:71], v[42:43], v[38:39] op_sel_hi:[0,1,1]
	ds_read_b128 v[36:39], v66 offset:1968
	ds_read_b128 v[40:43], v66 offset:1984
	v_pk_fma_f32 v[104:105], v[68:69], v[104:105], v[116:117] op_sel_hi:[0,1,1]
	v_pk_fma_f32 v[106:107], v[68:69], v[106:107], v[118:119] op_sel_hi:[0,1,1]
	v_pk_fma_f32 v[116:117], v[76:77], v[108:109], v[104:105] op_sel_hi:[0,1,1]
	v_pk_fma_f32 v[118:119], v[76:77], v[110:111], v[106:107] op_sel_hi:[0,1,1]
	ds_read_b128 v[104:107], v66 offset:2112
	ds_read_b128 v[108:111], v66 offset:2128
	s_waitcnt lgkmcnt(5)
	v_pk_fma_f32 v[28:29], v[74:75], v[28:29], v[116:117] op_sel_hi:[0,1,1]
	v_pk_fma_f32 v[30:31], v[74:75], v[30:31], v[118:119] op_sel_hi:[0,1,1]
	v_pk_fma_f32 v[16:17], v[86:87], v[16:17], v[88:89] op_sel_hi:[0,1,1]
	v_pk_fma_f32 v[28:29], v[72:73], v[60:61], v[28:29] op_sel_hi:[0,1,1]
	v_pk_fma_f32 v[30:31], v[72:73], v[62:63], v[30:31] op_sel_hi:[0,1,1]
	ds_read_b128 v[60:63], v66 offset:2288
	ds_read_b128 v[116:119], v66 offset:2304
	v_pk_fma_f32 v[16:17], v[84:85], v[20:21], v[16:17] op_sel_hi:[0,1,1]
	v_pk_fma_f32 v[18:19], v[86:87], v[18:19], v[94:95] op_sel_hi:[0,1,1]
	s_waitcnt lgkmcnt(3)
	v_pk_fma_f32 v[104:105], v[82:83], v[104:105], v[28:29] op_sel_hi:[0,1,1]
	v_pk_fma_f32 v[106:107], v[82:83], v[106:107], v[30:31] op_sel_hi:[0,1,1]
	ds_read_b128 v[28:31], v66 offset:2432
	v_pk_fma_f32 v[16:17], v[70:71], v[24:25], v[16:17] op_sel_hi:[0,1,1]
	v_pk_fma_f32 v[18:19], v[84:85], v[22:23], v[18:19] op_sel_hi:[0,1,1]
	v_pk_fma_f32 v[0:1], v[86:87], v[0:1], v[96:97] op_sel_hi:[0,1,1]
	v_pk_fma_f32 v[16:17], v[68:69], v[48:49], v[16:17] op_sel_hi:[0,1,1]
	v_pk_fma_f32 v[18:19], v[70:71], v[26:27], v[18:19] op_sel_hi:[0,1,1]
	ds_read_b128 v[20:23], v66 offset:2464
	v_pk_fma_f32 v[0:1], v[84:85], v[4:5], v[0:1] op_sel_hi:[0,1,1]
	v_pk_fma_f32 v[2:3], v[86:87], v[2:3], v[90:91] op_sel_hi:[0,1,1]
	v_pk_fma_f32 v[112:113], v[80:81], v[112:113], v[104:105] op_sel_hi:[0,1,1]
	v_pk_fma_f32 v[114:115], v[80:81], v[114:115], v[106:107] op_sel_hi:[0,1,1]
	ds_read_b128 v[104:107], v66 offset:2448
	v_subrev_u32_e32 v66, 0x16400, v66
	v_pk_fma_f32 v[16:17], v[76:77], v[120:121], v[16:17] op_sel_hi:[0,1,1]
	v_pk_fma_f32 v[18:19], v[68:69], v[50:51], v[18:19] op_sel_hi:[0,1,1]
	v_pk_fma_f32 v[0:1], v[70:71], v[8:9], v[0:1] op_sel_hi:[0,1,1]
	v_pk_fma_f32 v[2:3], v[84:85], v[6:7], v[2:3] op_sel_hi:[0,1,1]
	v_max_f32_e32 v4, v92, v93
	v_pk_fma_f32 v[16:17], v[74:75], v[100:101], v[16:17] op_sel_hi:[0,1,1]
	v_pk_fma_f32 v[18:19], v[76:77], v[122:123], v[18:19] op_sel_hi:[0,1,1]
	v_pk_fma_f32 v[0:1], v[68:69], v[12:13], v[0:1] op_sel_hi:[0,1,1]
	v_pk_fma_f32 v[2:3], v[70:71], v[10:11], v[2:3] op_sel_hi:[0,1,1]
	v_max3_f32 v4, v4, v98, v99
	v_pk_fma_f32 v[16:17], v[72:73], v[36:37], v[16:17] op_sel_hi:[0,1,1]
	v_pk_fma_f32 v[18:19], v[74:75], v[102:103], v[18:19] op_sel_hi:[0,1,1]
	v_pk_fma_f32 v[0:1], v[76:77], v[52:53], v[0:1] op_sel_hi:[0,1,1]
	v_pk_fma_f32 v[2:3], v[68:69], v[14:15], v[2:3] op_sel_hi:[0,1,1]
	v_max3_f32 v4, v4, v56, v57
	s_waitcnt lgkmcnt(2)
	v_pk_fma_f32 v[28:29], v[78:79], v[28:29], v[112:113] op_sel_hi:[0,1,1]
	v_pk_fma_f32 v[16:17], v[82:83], v[108:109], v[16:17] op_sel_hi:[0,1,1]
	v_pk_fma_f32 v[18:19], v[72:73], v[38:39], v[18:19] op_sel_hi:[0,1,1]
	v_pk_fma_f32 v[0:1], v[74:75], v[32:33], v[0:1] op_sel_hi:[0,1,1]
	v_pk_fma_f32 v[2:3], v[76:77], v[54:55], v[2:3] op_sel_hi:[0,1,1]
	v_max3_f32 v4, v4, v58, v59
	v_pk_fma_f32 v[30:31], v[78:79], v[30:31], v[114:115] op_sel_hi:[0,1,1]
	v_pk_fma_f32 v[16:17], v[80:81], v[60:61], v[16:17] op_sel_hi:[0,1,1]
	v_pk_fma_f32 v[18:19], v[82:83], v[110:111], v[18:19] op_sel_hi:[0,1,1]
	v_pk_fma_f32 v[0:1], v[72:73], v[40:41], v[0:1] op_sel_hi:[0,1,1]
	v_pk_fma_f32 v[2:3], v[74:75], v[34:35], v[2:3] op_sel_hi:[0,1,1]
	v_max3_f32 v4, v4, v28, v29
	s_waitcnt lgkmcnt(0)
	v_pk_fma_f32 v[16:17], v[78:79], v[104:105], v[16:17] op_sel_hi:[0,1,1]
	v_pk_fma_f32 v[18:19], v[80:81], v[62:63], v[18:19] op_sel_hi:[0,1,1]
	v_pk_fma_f32 v[0:1], v[82:83], v[44:45], v[0:1] op_sel_hi:[0,1,1]
	v_pk_fma_f32 v[2:3], v[72:73], v[42:43], v[2:3] op_sel_hi:[0,1,1]
	v_max3_f32 v4, v4, v30, v31
	v_pk_fma_f32 v[18:19], v[78:79], v[106:107], v[18:19] op_sel_hi:[0,1,1]
	v_pk_fma_f32 v[0:1], v[80:81], v[116:117], v[0:1] op_sel_hi:[0,1,1]
	v_pk_fma_f32 v[2:3], v[82:83], v[46:47], v[2:3] op_sel_hi:[0,1,1]
	v_max3_f32 v4, v4, v16, v17
	v_pk_fma_f32 v[0:1], v[78:79], v[20:21], v[0:1] op_sel_hi:[0,1,1]
	v_pk_fma_f32 v[2:3], v[80:81], v[118:119], v[2:3] op_sel_hi:[0,1,1]
	v_max3_f32 v4, v4, v18, v19
	v_pk_fma_f32 v[2:3], v[78:79], v[22:23], v[2:3] op_sel_hi:[0,1,1]
	v_max3_f32 v4, v4, v0, v1
	v_max3_f32 v4, v4, v2, v3
	s_nop 1
	v_mov_b32_dpp v5, v4 quad_perm:[1,0,3,2] row_mask:0xf bank_mask:0xf
	s_waitcnt lgkmcnt(0)
	v_max_f32_e32 v5, v5, v5
	v_max_f32_e32 v4, v4, v5
	v_sub_f32_e32 v5, v92, v4
	v_mul_f32_e32 v5, 0x3fb8aa3b, v5
	v_sub_f32_e32 v6, v93, v4
	v_exp_f32_e32 v5, v5
	v_mul_f32_e32 v6, 0x3fb8aa3b, v6
	v_sub_f32_e32 v7, v98, v4
	v_exp_f32_e32 v6, v6
	v_mul_f32_e32 v7, 0x3fb8aa3b, v7
	v_sub_f32_e32 v8, v99, v4
	v_exp_f32_e32 v7, v7
	v_mul_f32_e32 v8, 0x3fb8aa3b, v8
	v_exp_f32_e32 v8, v8
	v_add_f32_e32 v5, 0, v5
	v_add_f32_e32 v5, v5, v6
	v_sub_f32_e32 v6, v56, v4
	v_add_f32_e32 v5, v5, v7
	v_mul_f32_e32 v6, 0x3fb8aa3b, v6
	v_sub_f32_e32 v7, v57, v4
	v_add_f32_e32 v5, v5, v8
	v_exp_f32_e32 v6, v6
	v_mul_f32_e32 v7, 0x3fb8aa3b, v7
	v_sub_f32_e32 v8, v58, v4
	v_exp_f32_e32 v7, v7
	v_mul_f32_e32 v8, 0x3fb8aa3b, v8
	v_sub_f32_e32 v9, v59, v4
	v_exp_f32_e32 v8, v8
	v_mul_f32_e32 v9, 0x3fb8aa3b, v9
	v_exp_f32_e32 v9, v9
	v_add_f32_e32 v5, v5, v6
	v_sub_f32_e32 v6, v28, v4
	v_add_f32_e32 v5, v5, v7
	v_mul_f32_e32 v6, 0x3fb8aa3b, v6
	v_sub_f32_e32 v7, v29, v4
	v_add_f32_e32 v5, v5, v8
	v_exp_f32_e32 v6, v6
	v_mul_f32_e32 v7, 0x3fb8aa3b, v7
	v_sub_f32_e32 v8, v30, v4
	v_add_f32_e32 v5, v5, v9
	v_exp_f32_e32 v7, v7
	v_mul_f32_e32 v8, 0x3fb8aa3b, v8
	v_sub_f32_e32 v9, v31, v4
	v_exp_f32_e32 v8, v8
	v_mul_f32_e32 v9, 0x3fb8aa3b, v9
	v_exp_f32_e32 v9, v9
	v_add_f32_e32 v5, v5, v6
	v_sub_f32_e32 v6, v16, v4
	v_add_f32_e32 v5, v5, v7
	v_mul_f32_e32 v6, 0x3fb8aa3b, v6
	v_sub_f32_e32 v7, v17, v4
	v_add_f32_e32 v5, v5, v8
	v_exp_f32_e32 v6, v6
	v_mul_f32_e32 v7, 0x3fb8aa3b, v7
	v_sub_f32_e32 v8, v18, v4
	v_add_f32_e32 v5, v5, v9
	v_exp_f32_e32 v7, v7
	v_mul_f32_e32 v8, 0x3fb8aa3b, v8
	v_sub_f32_e32 v9, v19, v4
	v_exp_f32_e32 v8, v8
	v_mul_f32_e32 v9, 0x3fb8aa3b, v9
	v_exp_f32_e32 v9, v9
	v_add_f32_e32 v5, v5, v6
	v_sub_f32_e32 v6, v0, v4
	v_add_f32_e32 v5, v5, v7
	v_mul_f32_e32 v6, 0x3fb8aa3b, v6
	v_sub_f32_e32 v7, v1, v4
	v_add_f32_e32 v5, v5, v8
	v_exp_f32_e32 v6, v6
	v_mul_f32_e32 v7, 0x3fb8aa3b, v7
	v_sub_f32_e32 v8, v2, v4
	v_add_f32_e32 v5, v5, v9
	v_exp_f32_e32 v7, v7
	v_mul_f32_e32 v8, 0x3fb8aa3b, v8
	v_sub_f32_e32 v9, v3, v4
	v_exp_f32_e32 v8, v8
	v_mul_f32_e32 v9, 0x3fb8aa3b, v9
	v_exp_f32_e32 v9, v9
	v_add_f32_e32 v5, v5, v6
	v_add_f32_e32 v5, v5, v7
	v_add_f32_e32 v5, v5, v8
	v_add_f32_e32 v5, v5, v9
	s_nop 1
	v_mov_b32_dpp v6, v5 quad_perm:[1,0,3,2] row_mask:0xf bank_mask:0xf
	s_and_b64 exec, exec, s[8:9]
	s_cbranch_execz .LBB2_371
	s_waitcnt lgkmcnt(0)
	v_add_f32_e32 v5, v5, v6
	s_mov_b32 s0, 0x800000
	v_cmp_gt_f32_e32 vcc, s0, v5
	s_mov_b32 s0, 0x3f317217
	v_mov_b32_e32 v67, 0
	v_cndmask_b32_e64 v6, 0, 32, vcc
	v_ldexp_f32 v5, v5, v6
	v_log_f32_e32 v5, v5
	s_nop 0
	v_mul_f32_e32 v6, 0x3f317217, v5
	v_fma_f32 v6, v5, s0, -v6
	v_fmamk_f32 v6, v5, 0x3377d1cf, v6
	s_mov_b32 s0, 0x7f800000
	v_fmac_f32_e32 v6, 0x3f317217, v5
	v_cmp_lt_f32_e64 s[0:1], |v5|, s0
	s_nop 1
	v_cndmask_b32_e64 v5, v5, v6, s[0:1]
	v_mov_b32_e32 v6, 0x41b17218
	v_cndmask_b32_e32 v6, 0, v6, vcc
	v_sub_f32_e32 v5, v5, v6
	v_add_f32_e32 v10, v4, v5
	s_mov_b64 s[0:1], exec
	s_bcnt1_i32_b64 s94, exec
	s_mulk_i32 s94, 0x50
	s_lshl_b32 s92, s91, 5
	s_add_i32 s92, s92, s64
	s_mulk_i32 s92, 0xa0
	s_add_u32 s92, s52, s92
	s_addc_u32 s93, s53, 0
	s_mul_i32 s95, s91, 0x1400
	s_add_i32 s90, s95, 0x11940
	s_add_i32 s95, s95, 0x10000
	s_cmp_lt_u32 s91, 5
	s_cselect_b32 s95, s95, s90
	v_mbcnt_lo_u32_b32 v9, -1, 0
	v_mbcnt_hi_u32_b32 v9, -1, v9
	v_mul_u32_u24_e32 v8, 0x50, v9
	v_add_u32_e32 v8, s95, v8
	v_sub_f32_e32 v7, v99, v10
	v_sub_f32_e32 v6, v98, v10
	v_sub_f32_e32 v5, v93, v10
	v_sub_f32_e32 v4, v92, v10
	ds_write_b128 v8, v[4:7]
	v_sub_f32_e32 v3, v3, v10
	v_sub_f32_e32 v2, v2, v10
	v_sub_f32_e32 v7, v59, v10
	v_sub_f32_e32 v6, v58, v10
	v_sub_f32_e32 v5, v57, v10
	v_sub_f32_e32 v4, v56, v10
	ds_write_b128 v8, v[4:7] offset:16
	v_sub_f32_e32 v1, v1, v10
	v_sub_f32_e32 v0, v0, v10
	v_sub_f32_e32 v7, v31, v10
	v_sub_f32_e32 v6, v30, v10
	v_sub_f32_e32 v5, v29, v10
	v_sub_f32_e32 v4, v28, v10
	ds_write_b128 v8, v[4:7] offset:32
	ds_write_b128 v8, v[0:3] offset:64
	v_sub_f32_e32 v7, v19, v10
	v_sub_f32_e32 v6, v18, v10
	v_sub_f32_e32 v5, v17, v10
	v_sub_f32_e32 v4, v16, v10
	ds_write_b128 v8, v[4:7] offset:48
	s_mov_b64 exec, -1
	v_mbcnt_lo_u32_b32 v9, -1, 0
	v_mbcnt_hi_u32_b32 v9, -1, v9
	v_lshlrev_b32_e32 v9, 4, v9
	v_add_u32_e32 v8, s95, v9
	v_add_u32_e32 v11, 0x1000, v9
	s_waitcnt lgkmcnt(0)
	ds_read_b128 v[12:15], v8
	ds_read_b128 v[16:19], v8 offset:1024
	ds_read_b128 v[20:23], v8 offset:2048
	ds_read_b128 v[24:27], v8 offset:3072
	ds_read_b128 v[28:31], v8 offset:4096
	v_cmp_gt_i32_e32 vcc, s94, v9
	s_mov_b64 exec, vcc
	s_waitcnt lgkmcnt(4)
	global_store_dwordx4 v9, v[12:15], s[92:93]
	s_sub_i32 s94, s94, 0x400
	v_cmp_gt_i32_e32 vcc, s94, v9
	s_mov_b64 exec, vcc
	s_waitcnt lgkmcnt(3)
	global_store_dwordx4 v9, v[16:19], s[92:93] offset:1024
	s_sub_i32 s94, s94, 0x400
	v_cmp_gt_i32_e32 vcc, s94, v9
	s_mov_b64 exec, vcc
	s_waitcnt lgkmcnt(2)
	global_store_dwordx4 v9, v[20:23], s[92:93] offset:2048
	s_sub_i32 s94, s94, 0x400
	v_cmp_gt_i32_e32 vcc, s94, v9
	s_mov_b64 exec, vcc
	s_waitcnt lgkmcnt(1)
	global_store_dwordx4 v9, v[24:27], s[92:93] offset:3072
	s_sub_i32 s94, s94, 0x400
	v_cmp_gt_i32_e32 vcc, s94, v9
	s_mov_b64 exec, vcc
	s_waitcnt lgkmcnt(0)
	global_store_dwordx4 v11, v[28:31], s[92:93]
